# v82 + thin1 row loop prefetches two rows ahead (two landing register sets, next->cur copies after the stores)
# speedup vs baseline: 1.0032x; 1.0032x over previous
.LBB0_267:
	v_readlane_b32 s18, v252, 1
	v_readlane_b32 s2, v254, 39
	v_readlane_b32 s19, v252, 2
	s_waitcnt lgkmcnt(0)
	v_mov_b32_e32 v4, s2
	v_readlane_b32 s2, v254, 40
	s_barrier
	v_mbcnt_lo_u32_b32 v26, -1, 0
	v_mbcnt_hi_u32_b32 v26, -1, v26
	v_readlane_b32 s6, v252, 6
	v_mov_b32_e32 v5, s2
	ds_read_b32 v0, v4
	ds_read_b32 v1, v5
	v_readlane_b32 s2, v252, 7
	s_add_i32 s36, s6, s2
	s_lshl_b32 s96, s72, 6
	s_waitcnt lgkmcnt(1)
	v_readfirstlane_b32 s2, v0
	s_waitcnt lgkmcnt(0)
	v_readfirstlane_b32 s3, v1
	s_lshl_b64 s[54:55], s[96:97], 2
	v_lshlrev_b32_e32 v0, 2, v26
	s_add_u32 s2, s2, s54
	v_and_b32_e32 v16, 28, v0
	s_addc_u32 s3, s3, s55
	v_lshlrev_b32_e32 v160, 2, v16
	global_load_dwordx4 v[0:3], v160, s[2:3]
	ds_read_b32 v4, v4
	ds_read_b32 v5, v5
	v_ashrrev_i32_e32 v27, 31, v26
	v_lshlrev_b32_e32 v68, 3, v26
	s_waitcnt lgkmcnt(1)
	v_readfirstlane_b32 s2, v4
	s_waitcnt lgkmcnt(0)
	v_readfirstlane_b32 s3, v5
	s_add_u32 s2, s2, s54
	s_addc_u32 s3, s3, s55
	s_nop 2
	global_load_dwordx4 v[4:7], v160, s[2:3] offset:128
	v_readlane_b32 s2, v254, 41
	s_nop 1
	v_mov_b32_e32 v8, s2
	v_readlane_b32 s2, v254, 42
	ds_read_b32 v8, v8
	s_nop 0
	v_mov_b32_e32 v9, s2
	ds_read_b32 v10, v9
	v_and_b32_e32 v9, 31, v26
	s_waitcnt lgkmcnt(1)
	v_readfirstlane_b32 s2, v8
	v_lshlrev_b32_e32 v8, 3, v9
	s_waitcnt lgkmcnt(0)
	v_readfirstlane_b32 s3, v10
	s_add_u32 s2, s2, s54
	s_addc_u32 s3, s3, s55
	s_lshl_b32 s96, s72, 7
	s_nop 1
	global_load_dwordx2 v[28:29], v8, s[2:3]
	v_readlane_b32 s2, v254, 43
	s_lshl_b64 s[4:5], s[96:97], 2
	s_nop 0
	v_mov_b32_e32 v10, s2
	v_readlane_b32 s2, v254, 44
	ds_read_b32 v10, v10
	s_nop 0
	v_mov_b32_e32 v11, s2
	ds_read_b32 v11, v11
	s_waitcnt lgkmcnt(1)
	v_readfirstlane_b32 s2, v10
	s_waitcnt lgkmcnt(0)
	v_readfirstlane_b32 s3, v11
	s_add_u32 s2, s2, s4
	v_writelane_b32 v255, s4, 42
	s_addc_u32 s3, s3, s5
	v_lshlrev_b64 v[10:11], 3, v[26:27]
	v_lshl_add_u64 v[12:13], s[2:3], 0, v[10:11]
	v_readlane_b32 s2, v254, 45
	global_load_dwordx2 v[24:25], v[12:13], off
	s_lshl_b32 s96, s72, 8
	v_mov_b32_e32 v14, s2
	v_readlane_b32 s2, v254, 46
	ds_read_b32 v12, v14
	s_lshl_b64 s[50:51], s[96:97], 2
	v_mov_b32_e32 v15, s2
	ds_read_b32 v13, v15
	v_writelane_b32 v255, s5, 43
	s_waitcnt lgkmcnt(1)
	v_readfirstlane_b32 s2, v12
	s_waitcnt lgkmcnt(0)
	v_readfirstlane_b32 s3, v13
	s_add_u32 s2, s2, s50
	s_addc_u32 s3, s3, s51
	v_lshl_add_u64 v[12:13], s[2:3], 0, v[10:11]
	global_load_dwordx2 v[30:31], v[12:13], off
	ds_read_b32 v12, v14
	ds_read_b32 v13, v15
	s_waitcnt lgkmcnt(1)
	v_readfirstlane_b32 s2, v12
	s_waitcnt lgkmcnt(0)
	v_readfirstlane_b32 s3, v13
	s_add_u32 s2, s2, s50
	s_addc_u32 s3, s3, s51
	v_lshl_add_u64 v[10:11], s[2:3], 0, v[10:11]
	global_load_dwordx2 v[32:33], v[10:11], off offset:512
	v_readlane_b32 s2, v254, 47
	s_cmpk_gt_i32 s36, 0x7fff
	s_nop 0
	v_mov_b32_e32 v10, s2
	v_readlane_b32 s2, v254, 48
	ds_read_b32 v10, v10
	s_nop 0
	v_mov_b32_e32 v11, s2
	ds_read_b32 v11, v11
	s_waitcnt lgkmcnt(1)
	v_readfirstlane_b32 s2, v10
	s_waitcnt lgkmcnt(0)
	v_readfirstlane_b32 s3, v11
	s_cbranch_scc1 .LBB0_272
	s_add_u32 s22, s18, 0x100000
	s_addc_u32 s23, s19, 0
	s_add_u32 s38, s18, 0x140000
	s_addc_u32 s39, s19, 0
	s_lshl_b32 s7, s36, 4
	s_lshr_b32 s31, s36, 2
	s_and_b32 s10, s7, 0x3f0
	s_and_b32 s31, s31, 0x1f0
	s_or_b32 s11, s10, 0x70800
	s_or_b32 s33, s31, 0x70200
	v_cmp_lt_u32_e64 s[40:41], 15, v9
	v_mov_b32_e32 v10, s33
	v_mov_b32_e32 v11, s11
	v_cndmask_b32_e64 v10, v10, v11, s[40:41]
	v_lshlrev_b32_e32 v10, 2, v10
	v_mov_b32_e32 v11, v161
	v_and_b32_e32 v8, 56, v8
	v_mov_b32_e32 v9, v161
	v_lshl_add_u64 v[10:11], s[22:23], 0, v[10:11]
	v_lshl_add_u64 v[10:11], v[10:11], 0, v[8:9]
	s_or_b32 s11, s31, 0x70000
	global_load_dwordx2 v[50:51], v[10:11], off
	s_or_b32 s10, s10, 0x70400
	v_mov_b32_e32 v10, s11
	s_lshl_b32 s11, s36, 7
	v_mov_b32_e32 v11, s10
	s_lshl_b32 s10, s36, 5
	s_and_b32 s11, s11, 0x3ff80
	v_lshl_add_u64 v[36:37], s[38:39], 0, v[160:161]
	v_cndmask_b32_e64 v10, v10, v11, s[40:41]
	s_add_u32 s38, s38, s11
	v_lshlrev_b32_e32 v10, 2, v10
	v_mov_b32_e32 v11, v161
	s_addc_u32 s39, s39, 0
	v_lshl_add_u64 v[34:35], s[22:23], 0, v[160:161]
	v_lshl_add_u64 v[38:39], s[22:23], 0, v[8:9]
	v_lshl_add_u64 v[10:11], s[22:23], 0, v[10:11]
	s_add_u32 s22, s22, s11
	v_lshl_add_u64 v[8:9], v[10:11], 0, v[8:9]
	s_addc_u32 s23, s23, 0
	s_ashr_i32 s37, s36, 31
	s_mul_i32 s31, s36, 0x1a00
	global_load_dwordx2 v[44:45], v[8:9], off
	global_load_dwordx4 v[12:15], v160, s[22:23]
	s_mul_hi_i32 s11, s36, 0x1a00
	global_load_dwordx4 v[8:11], v160, s[38:39]
	s_add_u32 s22, s18, s31
	s_addc_u32 s23, s19, s11
	s_add_u32 s22, s22, 0x6400000
	s_addc_u32 s23, s23, 0
	v_lshlrev_b64 v[20:21], 2, v[26:27]
	v_and_b32_e32 v18, 0xffffffc0, v68
	v_lshl_add_u64 v[22:23], s[22:23], 0, v[20:21]
	s_movk_i32 s33, 0x1000
	v_ashrrev_i32_e32 v19, 31, v18
	v_add_co_u32_e32 v40, vcc, s33, v22
	v_lshlrev_b64 v[18:19], 1, v[18:19]
	s_nop 0
	v_addc_co_u32_e32 v41, vcc, 0, v23, vcc
	v_readlane_b32 s12, v255, 42
	global_load_dword v76, v[40:41], off offset:1024
	global_load_dword v69, v[22:23], off offset:3584
	global_load_dword v70, v[22:23], off offset:3328
	global_load_dword v73, v[22:23], off offset:3072
	v_lshl_add_u64 v[22:23], s[22:23], 0, v[18:19]
	v_lshlrev_b32_e32 v160, 1, v16
	v_readlane_b32 s13, v255, 43
	s_add_u32 s2, s2, s12
	v_lshl_add_u64 v[16:17], v[22:23], 0, v[160:161]
	s_addc_u32 s3, s3, s13
	global_load_dwordx2 v[60:61], v[16:17], off offset:1088
	global_load_dwordx2 v[62:63], v[16:17], off offset:1024
	v_lshl_add_u64 v[16:17], v[26:27], 3, s[2:3]
	global_load_dwordx2 v[40:41], v[16:17], off
	v_and_b32_e32 v16, 8, v26
	v_cmp_eq_u32_e64 s[42:43], 0, v16
	v_and_b32_e32 v16, 7, v26
	v_lshl_or_b32 v16, v16, 3, s31
	v_mov_b32_e32 v17, s11
	s_lshl_b64 s[2:3], s[36:37], 10
	v_lshl_add_u64 v[46:47], v[16:17], 0, v[18:19]
	v_mov_b32_e32 v16, 0x1a00
	v_lshl_add_u64 v[42:43], s[2:3], 0, v[20:21]
	v_mad_i64_i32 v[48:49], s[2:3], s36, v16, v[20:21]
	s_mov_b64 s[4:5], 0x200000
	s_mov_b32 s11, s36
	s_waitcnt vmcnt(10)
	v_mov_b64_e32 v[54:55], v[50:51]
	s_waitcnt vmcnt(9)
	v_mov_b64_e32 v[52:53], v[44:45]
	s_waitcnt vmcnt(8)
	v_mov_b64_e32 v[18:19], v[14:15]
	v_mov_b64_e32 v[16:17], v[12:13]
	s_waitcnt vmcnt(7)
	v_mov_b64_e32 v[22:23], v[10:11]
	v_mov_b64_e32 v[20:21], v[8:9]
	s_waitcnt vmcnt(6)
	v_mov_b32_e32 v75, v76
	s_waitcnt vmcnt(5)
	v_mov_b32_e32 v74, v69
	s_waitcnt vmcnt(4)
	v_mov_b32_e32 v72, v70
	s_waitcnt vmcnt(3)
	v_mov_b32_e32 v71, v73
	s_waitcnt vmcnt(2)
	v_mov_b64_e32 v[56:57], v[60:61]
	s_waitcnt vmcnt(1)
	v_mov_b64_e32 v[58:59], v[62:63]
	s_waitcnt vmcnt(0)
	v_lshl_add_u64 v[66:67], s[18:19], 0, v[46:47]
	v_lshl_add_u64 v[64:65], s[18:19], 0, v[48:49]
	s_and_b32 s22, s10, 0xffe0
	s_lshr_b32 s31, s11, 2
	v_add_co_u32_e32 v96, vcc, 0x7100000, v66
	s_lshl_b32 s96, s22, 2
	s_and_b32 s22, s7, 0x3f0
	s_and_b32 s31, s31, 0x1f0
	v_addc_co_u32_e32 v97, vcc, 0, v67, vcc
	s_or_b32 s23, s22, 0x70400
	s_or_b32 s33, s31, 0x70000
	v_add_co_u32_e32 v98, vcc, 0x7100000, v64
	v_mov_b32_e32 v102, s33
	v_mov_b32_e32 v103, s23
	s_or_b32 s22, s22, 0x70800
	s_or_b32 s23, s31, 0x70200
	v_addc_co_u32_e32 v99, vcc, 0, v65, vcc
	v_cndmask_b32_e64 v102, v102, v103, s[40:41]
	v_mov_b32_e32 v106, s23
	v_mov_b32_e32 v107, s22
	global_load_dwordx2 v[110:111], v[96:97], off offset:1024
	global_load_dwordx2 v[108:109], v[96:97], off offset:1088
	global_load_dword v112, v[98:99], off offset:3072
	global_load_dword v113, v[98:99], off offset:3328
	v_add_co_u32_e32 v96, vcc, 0x7101000, v64
	v_lshlrev_b32_e32 v160, 2, v102
	v_cndmask_b32_e64 v106, v106, v107, s[40:41]
	v_addc_co_u32_e32 v97, vcc, 0, v65, vcc
	v_lshl_add_u64 v[100:101], v[34:35], 0, s[96:97]
	v_lshl_add_u64 v[104:105], v[38:39], 0, v[160:161]
	v_lshlrev_b32_e32 v160, 2, v106
	global_load_dword v114, v[98:99], off offset:3584
	global_load_dword v115, v[96:97], off offset:1024
	s_nop 0
	global_load_dwordx4 v[96:99], v[100:101], off
	v_lshl_add_u64 v[100:101], v[36:37], 0, s[96:97]
	v_lshl_add_u64 v[106:107], v[38:39], 0, v[160:161]
	global_load_dwordx4 v[100:103], v[100:101], off
	s_nop 0
	global_load_dwordx2 v[104:105], v[104:105], off
	s_nop 0
	global_load_dwordx2 v[106:107], v[106:107], off
	s_mov_b32 s99, 1
	s_branch .LBB0_270
.LBB0_269:
	v_lshlrev_b32_e32 v78, 16, v63
	v_and_b32_e32 v79, 0xffff0000, v63
	v_lshlrev_b32_e32 v84, 16, v62
	v_and_b32_e32 v85, 0xffff0000, v62
	v_lshlrev_b32_e32 v62, 16, v60
	v_and_b32_e32 v63, 0xffff0000, v60
	v_lshlrev_b32_e32 v80, 16, v61
	v_and_b32_e32 v81, 0xffff0000, v61
	v_pk_mul_f32 v[60:61], v[62:63], v[62:63]
	v_pk_mul_f32 v[82:83], v[80:81], v[80:81]
	v_pk_fma_f32 v[60:61], v[84:85], v[84:85], v[60:61]
	v_pk_fma_f32 v[82:83], v[78:79], v[78:79], v[82:83]
	v_add_f32_e32 v60, v60, v61
	v_add_f32_e32 v60, v60, v82
	v_add_f32_e32 v60, v60, v83
	s_mov_b32 s22, 0x6400000
	s_addk_i32 s11, 0x800
	v_add_f32_dpp v60, v60, v60 quad_perm:[1,0,3,2] row_mask:0xf bank_mask:0xf bound_ctrl:1
	s_add_i32 s10, s10, 0x10000
	s_add_i32 s7, s7, 0x8000
	v_add_f32_dpp v60, v60, v60 quad_perm:[2,3,0,1] row_mask:0xf bank_mask:0xf bound_ctrl:1
	s_nop 1
	v_add_f32_dpp v60, v60, v60 row_half_mirror row_mask:0xf bank_mask:0xf bound_ctrl:1
	v_fmamk_f32 v60, v60, 0x3c800000, v240
	v_rsq_f32_e32 v60, v60
	s_nop 0
	v_pk_mul_f32 v[62:63], v[60:61], v[62:63] op_sel_hi:[0,1]
	v_pk_mul_f32 v[82:83], v[60:61], v[84:85] op_sel_hi:[0,1]
	v_pk_mul_f32 v[62:63], v[4:5], v[62:63]
	v_pk_mul_f32 v[82:83], v[0:1], v[82:83]
	v_pk_mul_f32 v[84:85], v[8:9], v[62:63]
	s_nop 0
	v_pk_fma_f32 v[84:85], v[12:13], v[82:83], v[84:85] neg_lo:[0,0,1] neg_hi:[0,0,1]
	v_pk_mul_f32 v[12:13], v[12:13], v[62:63]
	s_nop 0
	v_pk_fma_f32 v[8:9], v[8:9], v[82:83], v[12:13]
	v_pk_mul_f32 v[12:13], v[60:61], v[78:79] op_sel_hi:[0,1]
	v_pk_mul_f32 v[60:61], v[60:61], v[80:81] op_sel_hi:[0,1]
	v_pk_mul_f32 v[60:61], v[6:7], v[60:61]
	v_pk_mul_f32 v[12:13], v[2:3], v[12:13]
	v_pk_mul_f32 v[62:63], v[10:11], v[60:61]
	v_cvt_pk_bf16_f32 v8, v8, v9
	v_pk_fma_f32 v[62:63], v[14:15], v[12:13], v[62:63] neg_lo:[0,0,1] neg_hi:[0,0,1]
	v_pk_mul_f32 v[14:15], v[14:15], v[60:61]
	s_nop 0
	v_pk_fma_f32 v[10:11], v[10:11], v[12:13], v[14:15]
	v_lshlrev_b32_e32 v14, 16, v76
	v_and_b32_e32 v15, 0xffff0000, v76
	v_pk_mul_f32 v[60:61], v[14:15], v[14:15]
	v_cvt_pk_bf16_f32 v9, v10, v11
	v_add_f32_e32 v13, v60, v61
	v_cvt_pk_bf16_f32 v12, v84, v85
	s_nop 0
	v_add_f32_dpp v13, v13, v13 quad_perm:[1,0,3,2] row_mask:0xf bank_mask:0xf bound_ctrl:1
	s_nop 1
	v_add_f32_dpp v13, v13, v13 quad_perm:[2,3,0,1] row_mask:0xf bank_mask:0xf bound_ctrl:1
	s_nop 1
	v_add_f32_dpp v13, v13, v13 row_half_mirror row_mask:0xf bank_mask:0xf bound_ctrl:1
	s_nop 1
	v_add_f32_dpp v13, v13, v13 row_mirror row_mask:0xf bank_mask:0xf bound_ctrl:1
	v_mov_b32_e32 v60, v13
	s_nop 1
	v_permlane16_swap_b32_e32 v13, v60
	v_add_f32_e32 v13, v13, v60
	v_fmamk_f32 v13, v13, 0x3c800000, v240
	v_rsq_f32_e32 v60, v13
	v_cvt_pk_bf16_f32 v13, v62, v63
	v_pk_mul_f32 v[10:11], v[60:61], v[14:15] op_sel_hi:[0,1]
	v_pk_mul_f32 v[10:11], v[28:29], v[10:11]
	v_lshlrev_b32_e32 v60, 16, v70
	v_and_b32_e32 v61, 0xffff0000, v70
	v_mov_b32_dpp v14, v10 row_ror:8 row_mask:0xf bank_mask:0xf bound_ctrl:1
	v_mov_b32_dpp v15, v11 row_ror:8 row_mask:0xf bank_mask:0xf bound_ctrl:1
	v_pk_mul_f32 v[14:15], v[50:51], v[14:15]
	v_lshlrev_b32_e32 v50, 16, v73
	v_and_b32_e32 v51, 0xffff0000, v73
	v_pk_mul_f32 v[76:77], v[50:51], v[50:51]
	v_pk_mul_f32 v[62:63], v[60:61], v[60:61]
	v_add_f32_e32 v70, v76, v77
	v_add_f32_e32 v62, v70, v62
	v_add_f32_e32 v62, v63, v62
	v_cndmask_b32_e64 v15, v15, -v15, s[42:43]
	v_cndmask_b32_e64 v14, v14, -v14, s[42:43]
	v_add_f32_dpp v62, v62, v62 quad_perm:[1,0,3,2] row_mask:0xf bank_mask:0xf bound_ctrl:1
	v_pk_fma_f32 v[10:11], v[44:45], v[10:11], v[14:15]
	s_nop 0
	s_nop 0
	v_add_f32_dpp v62, v62, v62 quad_perm:[2,3,0,1] row_mask:0xf bank_mask:0xf bound_ctrl:1
	s_nop 0
	s_nop 0
	s_nop 0
	s_nop 0
	v_add_f32_dpp v62, v62, v62 row_half_mirror row_mask:0xf bank_mask:0xf bound_ctrl:1
	s_nop 1
	v_add_f32_dpp v62, v62, v62 row_mirror row_mask:0xf bank_mask:0xf bound_ctrl:1
	v_mov_b32_e32 v63, v62
	s_nop 1
	v_permlane16_swap_b32_e32 v62, v63
	v_add_f32_e32 v62, v62, v63
	v_mov_b32_e32 v63, v62
	s_nop 1
	v_permlane32_swap_b32_e32 v62, v63
	v_add_f32_e32 v62, v62, v63
	v_fmamk_f32 v62, v62, 0x3b800000, v240
	v_rsq_f32_e32 v62, v62
	v_cvt_pk_bf16_f32 v63, v10, v11
	v_pk_mul_f32 v[10:11], v[62:63], v[50:51] op_sel_hi:[0,1]
	v_pk_mul_f32 v[10:11], v[30:31], v[10:11]
	v_pk_mul_f32 v[44:45], v[62:63], v[60:61] op_sel_hi:[0,1]
	v_cvt_pk_bf16_f32 v50, v10, v11
	v_lshlrev_b32_e32 v10, 16, v69
	v_and_b32_e32 v11, 0xffff0000, v69
	v_pk_mul_f32 v[14:15], v[10:11], v[10:11]
	v_pk_mul_f32 v[44:45], v[32:33], v[44:45]
	v_add_f32_e32 v14, v14, v15
	s_nop 0
	s_nop 0
	v_add_f32_dpp v14, v14, v14 quad_perm:[1,0,3,2] row_mask:0xf bank_mask:0xf bound_ctrl:1
	s_nop 1
	v_add_f32_dpp v14, v14, v14 quad_perm:[2,3,0,1] row_mask:0xf bank_mask:0xf bound_ctrl:1
	s_nop 1
	v_add_f32_dpp v14, v14, v14 row_half_mirror row_mask:0xf bank_mask:0xf bound_ctrl:1
	s_nop 1
	v_add_f32_dpp v14, v14, v14 row_mirror row_mask:0xf bank_mask:0xf bound_ctrl:1
	v_mov_b32_e32 v15, v14
	s_nop 1
	v_permlane16_swap_b32_e32 v14, v15
	v_add_f32_e32 v14, v14, v15
	v_mov_b32_e32 v15, v14
	s_nop 1
	v_permlane32_swap_b32_e32 v14, v15
	v_add_f32_e32 v14, v14, v15
	v_fmamk_f32 v14, v14, 0x3c000000, v240
	v_rsq_f32_e32 v14, v14
	v_cvt_pk_bf16_f32 v15, v44, v45
	s_nop 0
	s_nop 0
	v_pk_mul_f32 v[10:11], v[14:15], v[10:11] op_sel_hi:[0,1]
	s_nop 0
	v_pk_mul_f32 v[10:11], v[40:41], v[10:11]
	s_nop 0
	v_cvt_pk_bf16_f32 v14, v10, v11
	v_add_co_u32_e32 v10, vcc, s22, v66
	s_mov_b32 s22, 0x6401000
	s_nop 0
	v_addc_co_u32_e32 v11, vcc, 0, v67, vcc
	s_cmpk_gt_i32 s11, 0x77ff
	s_cbranch_scc1 .Lt1_w0
	s_waitcnt vmcnt(10)
	s_branch .Lt1_wd

.Lt1_wd:
	global_store_dwordx2 v[10:11], v[12:13], off offset:1024
	global_store_dwordx2 v[10:11], v[8:9], off offset:1088
	v_add_co_u32_e32 v8, vcc, s22, v64
	s_mov_b64 s[22:23], 0xd00000
	s_nop 0
	v_addc_co_u32_e32 v9, vcc, 0, v65, vcc
	global_store_dword v[8:9], v63, off offset:1024
	v_lshl_add_u64 v[8:9], s[18:19], 0, v[42:43]
	v_add_co_u32_e32 v8, vcc, 0x1d400000, v8
	v_lshl_add_u64 v[42:43], v[42:43], 0, s[4:5]
	s_nop 0
	v_addc_co_u32_e32 v9, vcc, 0, v9, vcc
	global_store_dword v[8:9], v50, off
	global_store_dword v[8:9], v15, off offset:256
	global_store_dword v[8:9], v14, off offset:512
	global_store_dword v[8:9], v161, off offset:768
	v_lshl_add_u64 v[46:47], v[46:47], 0, s[22:23]
	v_lshl_add_u64 v[48:49], v[48:49], 0, s[22:23]
.Lt1_copy:
	s_cmp_eq_u32 s99, 0
	s_cbranch_scc1 .Lt1_copy_n1
	v_mov_b32_e32 v73, v112
	v_mov_b32_e32 v70, v113
	v_mov_b32_e32 v76, v115
	v_mov_b32_e32 v69, v114
	v_mov_b64_e32 v[60:61], v[108:109]
	v_mov_b64_e32 v[44:45], v[104:105]
	v_mov_b64_e32 v[12:13], v[96:97]
	v_mov_b64_e32 v[8:9], v[100:101]
	v_mov_b64_e32 v[62:63], v[110:111]
	v_mov_b64_e32 v[14:15], v[98:99]
	v_mov_b64_e32 v[10:11], v[102:103]
	v_mov_b64_e32 v[50:51], v[106:107]
	s_mov_b32 s99, 0
	s_branch .Lt1_latch
.Lt1_copy_n1:
	v_mov_b32_e32 v73, v71
	v_mov_b32_e32 v70, v72
	v_mov_b32_e32 v76, v75
	v_mov_b32_e32 v69, v74
	v_mov_b64_e32 v[60:61], v[56:57]
	v_mov_b64_e32 v[44:45], v[52:53]
	v_mov_b64_e32 v[12:13], v[16:17]
	v_mov_b64_e32 v[8:9], v[20:21]
	v_mov_b64_e32 v[62:63], v[58:59]
	v_mov_b64_e32 v[14:15], v[18:19]
	v_mov_b64_e32 v[10:11], v[22:23]
	v_mov_b64_e32 v[50:51], v[54:55]
	s_mov_b32 s99, 1
.Lt1_latch:
	s_and_b64 vcc, exec, s[2:3]
	s_cbranch_vccnz .LBB0_272
.LBB0_270:
	s_cmpk_gt_i32 s11, 0x77ff
	s_cselect_b64 s[2:3], -1, 0
	v_lshl_add_u64 v[66:67], s[18:19], 0, v[46:47]
	v_lshl_add_u64 v[64:65], s[18:19], 0, v[48:49]
	s_cmpk_gt_i32 s11, 0x6fff
	s_cbranch_scc1 .LBB0_269
	s_cmp_eq_u32 s99, 0
	s_cbranch_scc1 .Lt1_issue_n2
	s_and_b32 s22, s10, 0xffe0
	s_lshr_b32 s31, s11, 2
	v_add_co_u32_e32 v16, vcc, 0x7e00000, v66
	s_lshl_b32 s96, s22, 2
	s_and_b32 s22, s7, 0x3f0
	s_and_b32 s31, s31, 0x1f0
	v_addc_co_u32_e32 v17, vcc, 0, v67, vcc
	s_or_b32 s23, s22, 0x70400
	s_or_b32 s33, s31, 0x70000
	v_add_co_u32_e32 v18, vcc, 0x7e00000, v64
	v_mov_b32_e32 v22, s33
	v_mov_b32_e32 v23, s23
	s_or_b32 s22, s22, 0x70800
	s_or_b32 s23, s31, 0x70200
	v_addc_co_u32_e32 v19, vcc, 0, v65, vcc
	v_cndmask_b32_e64 v22, v22, v23, s[40:41]
	v_mov_b32_e32 v54, s23
	v_mov_b32_e32 v55, s22
	global_load_dwordx2 v[58:59], v[16:17], off offset:1024
	global_load_dwordx2 v[56:57], v[16:17], off offset:1088
	global_load_dword v71, v[18:19], off offset:3072
	global_load_dword v72, v[18:19], off offset:3328
	v_add_co_u32_e32 v16, vcc, 0x7e01000, v64
	v_lshlrev_b32_e32 v160, 2, v22
	v_cndmask_b32_e64 v54, v54, v55, s[40:41]
	v_addc_co_u32_e32 v17, vcc, 0, v65, vcc
	v_lshl_add_u64 v[20:21], v[34:35], 0, s[96:97]
	v_lshl_add_u64 v[52:53], v[38:39], 0, v[160:161]
	v_lshlrev_b32_e32 v160, 2, v54
	global_load_dword v74, v[18:19], off offset:3584
	global_load_dword v75, v[16:17], off offset:1024
	s_nop 0
	global_load_dwordx4 v[16:19], v[20:21], off
	v_lshl_add_u64 v[20:21], v[36:37], 0, s[96:97]
	v_lshl_add_u64 v[54:55], v[38:39], 0, v[160:161]
	global_load_dwordx4 v[20:23], v[20:21], off
	s_nop 0
	global_load_dwordx2 v[52:53], v[52:53], off
	s_nop 0
	global_load_dwordx2 v[54:55], v[54:55], off
	s_branch .LBB0_269
.Lt1_issue_n2:
	s_and_b32 s22, s10, 0xffe0
	s_lshr_b32 s31, s11, 2
	v_add_co_u32_e32 v96, vcc, 0x7e00000, v66
	s_lshl_b32 s96, s22, 2
	s_and_b32 s22, s7, 0x3f0
	s_and_b32 s31, s31, 0x1f0
	v_addc_co_u32_e32 v97, vcc, 0, v67, vcc
	s_or_b32 s23, s22, 0x70400
	s_or_b32 s33, s31, 0x70000
	v_add_co_u32_e32 v98, vcc, 0x7e00000, v64
	v_mov_b32_e32 v102, s33
	v_mov_b32_e32 v103, s23
	s_or_b32 s22, s22, 0x70800
	s_or_b32 s23, s31, 0x70200
	v_addc_co_u32_e32 v99, vcc, 0, v65, vcc
	v_cndmask_b32_e64 v102, v102, v103, s[40:41]
	v_mov_b32_e32 v106, s23
	v_mov_b32_e32 v107, s22
	global_load_dwordx2 v[110:111], v[96:97], off offset:1024
	global_load_dwordx2 v[108:109], v[96:97], off offset:1088
	global_load_dword v112, v[98:99], off offset:3072
	global_load_dword v113, v[98:99], off offset:3328
	v_add_co_u32_e32 v96, vcc, 0x7e01000, v64
	v_lshlrev_b32_e32 v160, 2, v102
	v_cndmask_b32_e64 v106, v106, v107, s[40:41]
	v_addc_co_u32_e32 v97, vcc, 0, v65, vcc
	v_lshl_add_u64 v[100:101], v[34:35], 0, s[96:97]
	v_lshl_add_u64 v[104:105], v[38:39], 0, v[160:161]
	v_lshlrev_b32_e32 v160, 2, v106
	global_load_dword v114, v[98:99], off offset:3584
	global_load_dword v115, v[96:97], off offset:1024
	s_nop 0
	global_load_dwordx4 v[96:99], v[100:101], off
	v_lshl_add_u64 v[100:101], v[36:37], 0, s[96:97]
	v_lshl_add_u64 v[106:107], v[38:39], 0, v[160:161]
	global_load_dwordx4 v[100:103], v[100:101], off
	s_nop 0
	global_load_dwordx2 v[104:105], v[104:105], off
	s_nop 0
	global_load_dwordx2 v[106:107], v[106:107], off
	s_branch .LBB0_269
